# out-proj epilogue: residual x loads marked non-temporal (x is dead after this read) so the freshly written x1 stays cached for the router and the MoE gather
# speedup vs baseline: 1.0107x; 1.0107x over previous
; #define PG8_STAGE_A(bufoff, soff, voff) do { _Pragma("unroll") for (int _i = 0; _i < 2; ++_i) \
;         __builtin_amdgcn_raw_ptr_buffer_load_lds(rsA, (LAS void*)(lds + (bufoff) + ldsw + _i * 8192), 16, (voff)[_i], (soff), 0, 0); } while (0)
; #define PG8_STAGE_B(bufoff, soff) do { _Pragma("unroll") for (int _i = 0; _i < 2; ++_i) \
;         __builtin_amdgcn_raw_ptr_buffer_load_lds(rsB, (LAS void*)(lds + (bufoff) + ldsw + _i * 8192), 16, voffB[_i], (soff), 0, 0); } while (0)
; #define PG8_LDA(dst, b, h) do { _Pragma("unroll") for (int m = 0; m < 4; ++m) dst[m] = PG8_LD8(lds + PG8_SA(b, h) + aoff + m * 2048); } while (0)
; #define PG8_LDB(dst, b, h) do { _Pragma("unroll") for (int n = 0; n < 2; ++n) dst[n] = PG8_LD8(lds + PG8_SB(b, h) + boff + n * 2048); } while (0)
; #define PG8_WAIT_V(n) asm volatile("s_waitcnt vmcnt(" #n ")" ::: "memory")
; #define PG8_WAIT_L(n) asm volatile("s_waitcnt lgkmcnt(" #n ")" ::: "memory")
; #define PG8_BAR __builtin_amdgcn_s_barrier()
; #define PG8_SCHED __builtin_amdgcn_sched_barrier(0)
; template <class Epi, class Sched, bool GATHER, bool ALIGN_EPI, bool SP2, bool FP8>
; __device__ __forceinline__ void gemm_phase(LAS unsigned char* lds, const Gemm g, const Sched& S, const Epi& E) {
;     ...
;             PG8_LDB(B0, 0, 0); PG8_LDB(B1, 0, 1); PG8_SCHED; PG8_LDA(At, 0, 0); PG8_STAGE_A(PG8_SA(1, 1), a1, vA1);
;             PG8_WAIT_V(8); PG8_WAIT_L(0); PG8_BAR; PG8_MMA(0, 0, At, B0); PG8_MMA(0, 1, At, B1); PG8_BAR; PG8_SCHED;
;             PG8_LDA(At, 0, 1); PG8_STAGE_B(PG8_SB(0, 0), b2); PG8_STAGE_B(PG8_SB(0, 1), b2 + hstep); PG8_STAGE_A(PG8_SA(0, 0), a2, va20);
;             PG8_WAIT_V(8); PG8_WAIT_L(0); PG8_BAR; PG8_MMA(1, 0, At, B0); PG8_MMA(1, 1, At, B1); PG8_BAR; PG8_SCHED;
.LBB0_708:
	ds_read_b128 v[158:161], v172
	ds_read_b128 v[154:157], v172 offset:1024
	ds_read_b128 v[150:153], v172 offset:2048
	ds_read_b128 v[146:149], v172 offset:3072
	ds_read_b128 v[142:145], v173
	ds_read_b128 v[138:141], v173 offset:1024
	ds_read_b128 v[134:137], v173 offset:2048
	ds_read_b128 v[130:133], v173 offset:3072
	s_add_i32 s10, s77, 0x80
	s_cmp_eq_u32 s79, 28
	s_cselect_b32 s82, s75, s10
	s_cselect_b32 s81, s76, s78
	s_or_b32 s80, s82, 0x80
	s_mov_b32 m0, s52
	ds_read_b128 v[178:181], v174
	ds_read_b128 v[182:185], v174 offset:1024
	ds_read_b128 v[186:189], v174 offset:2048
	ds_read_b128 v[190:193], v174 offset:3072
	ds_read_b128 v[194:197], v174 offset:4096
	ds_read_b128 v[198:201], v174 offset:5120
	ds_read_b128 v[202:205], v174 offset:6144
	ds_read_b128 v[206:209], v174 offset:7168
	buffer_load_dwordx4 v170, s[4:7], s77 offen lds
	s_mov_b32 m0, s53
	s_nop 0
	buffer_load_dwordx4 v171, s[4:7], s77 offen lds
	s_waitcnt vmcnt(8)
	s_waitcnt lgkmcnt(0)
	s_barrier
	s_setprio 1
	s_waitcnt lgkmcnt(0)
	v_mfma_f32_16x16x32_bf16 v[126:129], v[158:161], v[178:181], v[126:129]
	s_nop 0
	v_mfma_f32_16x16x32_bf16 v[126:129], v[154:157], v[182:185], v[126:129]
	v_mfma_f32_16x16x32_bf16 v[122:125], v[150:153], v[178:181], v[122:125]
	s_nop 0
	v_mfma_f32_16x16x32_bf16 v[122:125], v[146:149], v[182:185], v[122:125]
	v_mfma_f32_16x16x32_bf16 v[110:113], v[158:161], v[186:189], v[110:113]
	s_nop 0
	v_mfma_f32_16x16x32_bf16 v[110:113], v[154:157], v[190:193], v[110:113]
	v_mfma_f32_16x16x32_bf16 v[106:109], v[150:153], v[186:189], v[106:109]
	s_nop 0
	v_mfma_f32_16x16x32_bf16 v[106:109], v[146:149], v[190:193], v[106:109]
	v_mfma_f32_16x16x32_bf16 v[94:97], v[158:161], v[194:197], v[94:97]
	s_nop 0
	v_mfma_f32_16x16x32_bf16 v[94:97], v[154:157], v[198:201], v[94:97]
	v_mfma_f32_16x16x32_bf16 v[90:93], v[150:153], v[194:197], v[90:93]
	s_nop 0
	v_mfma_f32_16x16x32_bf16 v[90:93], v[146:149], v[198:201], v[90:93]
	v_mfma_f32_16x16x32_bf16 v[78:81], v[158:161], v[202:205], v[78:81]
	s_nop 0
	v_mfma_f32_16x16x32_bf16 v[78:81], v[154:157], v[206:209], v[78:81]
	v_mfma_f32_16x16x32_bf16 v[74:77], v[150:153], v[202:205], v[74:77]
	s_nop 0
	v_mfma_f32_16x16x32_bf16 v[74:77], v[146:149], v[206:209], v[74:77]
	s_setprio 0
	s_setprio 1
	v_mfma_f32_16x16x32_bf16 v[118:121], v[142:145], v[178:181], v[118:121]
	s_nop 0
	v_mfma_f32_16x16x32_bf16 v[118:121], v[138:141], v[182:185], v[118:121]
	v_mfma_f32_16x16x32_bf16 v[114:117], v[134:137], v[178:181], v[114:117]
	s_nop 0
	v_mfma_f32_16x16x32_bf16 v[114:117], v[130:133], v[182:185], v[114:117]
	v_mfma_f32_16x16x32_bf16 v[102:105], v[142:145], v[186:189], v[102:105]
	s_nop 0
	v_mfma_f32_16x16x32_bf16 v[102:105], v[138:141], v[190:193], v[102:105]
	v_mfma_f32_16x16x32_bf16 v[98:101], v[134:137], v[186:189], v[98:101]
	s_nop 0
	v_mfma_f32_16x16x32_bf16 v[98:101], v[130:133], v[190:193], v[98:101]
	v_mfma_f32_16x16x32_bf16 v[86:89], v[142:145], v[194:197], v[86:89]
	s_nop 0
	v_mfma_f32_16x16x32_bf16 v[86:89], v[138:141], v[198:201], v[86:89]
	v_mfma_f32_16x16x32_bf16 v[82:85], v[134:137], v[194:197], v[82:85]
	s_nop 0
	v_mfma_f32_16x16x32_bf16 v[82:85], v[130:133], v[198:201], v[82:85]
	v_mfma_f32_16x16x32_bf16 v[70:73], v[142:145], v[202:205], v[70:73]
	s_nop 0
	v_mfma_f32_16x16x32_bf16 v[70:73], v[138:141], v[206:209], v[70:73]
	v_mfma_f32_16x16x32_bf16 v[66:69], v[134:137], v[202:205], v[66:69]
	s_nop 0
	v_mfma_f32_16x16x32_bf16 v[66:69], v[130:133], v[206:209], v[66:69]
	s_setprio 0
	s_barrier
	s_mov_b32 m0, s37
	s_mov_b32 s10, s6
	s_mov_b32 s11, s7
	ds_read_b128 v[178:181], v174 offset:16384
	ds_read_b128 v[182:185], v174 offset:17408
	ds_read_b128 v[186:189], v174 offset:18432
	ds_read_b128 v[190:193], v174 offset:19456
	ds_read_b128 v[194:197], v174 offset:20480
	ds_read_b128 v[198:201], v174 offset:21504
	ds_read_b128 v[202:205], v174 offset:22528
	ds_read_b128 v[206:209], v174 offset:23552
	buffer_load_dwordx4 v1, s[8:11], s81 offen lds
	s_mov_b32 m0, s38
	s_add_i32 s83, s81, 0x80000
	buffer_load_dwordx4 v163, s[8:11], s81 offen lds
	s_mov_b32 m0, s39
	s_nop 0
	buffer_load_dwordx4 v1, s[8:11], s83 offen lds
	s_mov_b32 m0, s40
	s_nop 0
	buffer_load_dwordx4 v163, s[8:11], s83 offen lds
	s_mov_b32 m0, s36
	s_nop 0
	buffer_load_dwordx4 v168, s[4:7], s82 offen lds
	s_mov_b32 m0, s41
	s_nop 0
	buffer_load_dwordx4 v169, s[4:7], s82 offen lds
	s_waitcnt vmcnt(8)
	s_waitcnt lgkmcnt(0)
	s_barrier
; #define PG8_STAGE_A(bufoff, soff, voff) do { _Pragma("unroll") for (int _i = 0; _i < 2; ++_i) \
;         __builtin_amdgcn_raw_ptr_buffer_load_lds(rsA, (LAS void*)(lds + (bufoff) + ldsw + _i * 8192), 16, (voff)[_i], (soff), 0, 0); } while (0)
; #define PG8_LDA(dst, b, h) do { _Pragma("unroll") for (int m = 0; m < 4; ++m) dst[m] = PG8_LD8(lds + PG8_SA(b, h) + aoff + m * 2048); } while (0)
; #define PG8_LDB(dst, b, h) do { _Pragma("unroll") for (int n = 0; n < 2; ++n) dst[n] = PG8_LD8(lds + PG8_SB(b, h) + boff + n * 2048); } while (0)
; #define PG8_WAIT_V(n) asm volatile("s_waitcnt vmcnt(" #n ")" ::: "memory")
; #define PG8_WAIT_L(n) asm volatile("s_waitcnt lgkmcnt(" #n ")" ::: "memory")
; #define PG8_BAR __builtin_amdgcn_s_barrier()
; #define PG8_SCHED __builtin_amdgcn_sched_barrier(0)
; template <class Epi, class Sched, bool GATHER, bool ALIGN_EPI, bool SP2, bool FP8>
; __device__ __forceinline__ void gemm_phase(LAS unsigned char* lds, const Gemm g, const Sched& S, const Epi& E) {
;     ...
;             PG8_WAIT_V(8); PG8_WAIT_L(0); PG8_BAR; PG8_MMA(1, 0, At, B0); PG8_MMA(1, 1, At, B1); PG8_BAR; PG8_SCHED;
;             PG8_LDB(B0, 1, 0); PG8_LDB(B1, 1, 1); PG8_SCHED; PG8_LDA(At, 1, 0); PG8_STAGE_A(PG8_SA(0, 1), a2, va21);
;             PG8_WAIT_V(8); PG8_WAIT_L(0); PG8_BAR; PG8_MMA(0, 0, At, B0); PG8_MMA(0, 1, At, B1); PG8_BAR; PG8_SCHED;
	s_setprio 1
	s_waitcnt lgkmcnt(7)
	v_mfma_f32_16x16x32_bf16 v[62:65], v[158:161], v[178:181], v[62:65]
	s_waitcnt lgkmcnt(6)
	v_mfma_f32_16x16x32_bf16 v[62:65], v[154:157], v[182:185], v[62:65]
	v_mfma_f32_16x16x32_bf16 v[58:61], v[150:153], v[178:181], v[58:61]
	s_nop 0
	v_mfma_f32_16x16x32_bf16 v[58:61], v[146:149], v[182:185], v[58:61]
	s_waitcnt lgkmcnt(5)
	v_mfma_f32_16x16x32_bf16 v[46:49], v[158:161], v[186:189], v[46:49]
	s_waitcnt lgkmcnt(4)
	v_mfma_f32_16x16x32_bf16 v[46:49], v[154:157], v[190:193], v[46:49]
	v_mfma_f32_16x16x32_bf16 v[42:45], v[150:153], v[186:189], v[42:45]
	s_nop 0
	v_mfma_f32_16x16x32_bf16 v[42:45], v[146:149], v[190:193], v[42:45]
	s_waitcnt lgkmcnt(3)
	v_mfma_f32_16x16x32_bf16 v[30:33], v[158:161], v[194:197], v[30:33]
	s_waitcnt lgkmcnt(2)
	v_mfma_f32_16x16x32_bf16 v[30:33], v[154:157], v[198:201], v[30:33]
	v_mfma_f32_16x16x32_bf16 v[26:29], v[150:153], v[194:197], v[26:29]
	s_nop 0
	v_mfma_f32_16x16x32_bf16 v[26:29], v[146:149], v[198:201], v[26:29]
	s_waitcnt lgkmcnt(1)
	v_mfma_f32_16x16x32_bf16 v[14:17], v[158:161], v[202:205], v[14:17]
	s_waitcnt lgkmcnt(0)
	v_mfma_f32_16x16x32_bf16 v[14:17], v[154:157], v[206:209], v[14:17]
	v_mfma_f32_16x16x32_bf16 v[10:13], v[150:153], v[202:205], v[10:13]
	s_nop 0
	v_mfma_f32_16x16x32_bf16 v[10:13], v[146:149], v[206:209], v[10:13]
	s_setprio 0
	s_setprio 1
	v_mfma_f32_16x16x32_bf16 v[54:57], v[142:145], v[178:181], v[54:57]
	s_nop 0
	v_mfma_f32_16x16x32_bf16 v[54:57], v[138:141], v[182:185], v[54:57]
	v_mfma_f32_16x16x32_bf16 v[50:53], v[134:137], v[178:181], v[50:53]
	s_nop 0
	v_mfma_f32_16x16x32_bf16 v[50:53], v[130:133], v[182:185], v[50:53]
	v_mfma_f32_16x16x32_bf16 v[38:41], v[142:145], v[186:189], v[38:41]
	s_nop 0
	v_mfma_f32_16x16x32_bf16 v[38:41], v[138:141], v[190:193], v[38:41]
	v_mfma_f32_16x16x32_bf16 v[34:37], v[134:137], v[186:189], v[34:37]
	s_nop 0
	v_mfma_f32_16x16x32_bf16 v[34:37], v[130:133], v[190:193], v[34:37]
	v_mfma_f32_16x16x32_bf16 v[22:25], v[142:145], v[194:197], v[22:25]
	s_nop 0
	v_mfma_f32_16x16x32_bf16 v[22:25], v[138:141], v[198:201], v[22:25]
	v_mfma_f32_16x16x32_bf16 v[18:21], v[134:137], v[194:197], v[18:21]
	s_nop 0
	v_mfma_f32_16x16x32_bf16 v[18:21], v[130:133], v[198:201], v[18:21]
	v_mfma_f32_16x16x32_bf16 v[6:9], v[142:145], v[202:205], v[6:9]
	s_nop 0
	v_mfma_f32_16x16x32_bf16 v[6:9], v[138:141], v[206:209], v[6:9]
	v_mfma_f32_16x16x32_bf16 v[2:5], v[134:137], v[202:205], v[2:5]
	s_nop 0
	v_mfma_f32_16x16x32_bf16 v[2:5], v[130:133], v[206:209], v[2:5]
	s_setprio 0
	s_barrier
	ds_read_b128 v[130:133], v175
	ds_read_b128 v[134:137], v175 offset:1024
	ds_read_b128 v[138:141], v175 offset:2048
	ds_read_b128 v[142:145], v175 offset:3072
	ds_read_b128 v[146:149], v176
	ds_read_b128 v[150:153], v176 offset:1024
	ds_read_b128 v[154:157], v176 offset:2048
	ds_read_b128 v[158:161], v176 offset:3072
	s_mov_b32 m0, s42
	ds_read_b128 v[178:181], v174 offset:32768
	ds_read_b128 v[182:185], v174 offset:33792
	ds_read_b128 v[186:189], v174 offset:34816
	ds_read_b128 v[190:193], v174 offset:35840
	ds_read_b128 v[194:197], v174 offset:36864
	ds_read_b128 v[198:201], v174 offset:37888
	ds_read_b128 v[202:205], v174 offset:38912
	ds_read_b128 v[206:209], v174 offset:39936
	buffer_load_dwordx4 v170, s[4:7], s82 offen lds
	s_mov_b32 m0, s43
	s_nop 0
	buffer_load_dwordx4 v171, s[4:7], s82 offen lds
	s_waitcnt vmcnt(8)
	s_waitcnt lgkmcnt(0)
	s_barrier
	s_setprio 1
	s_waitcnt lgkmcnt(7)
	v_mfma_f32_16x16x32_bf16 v[126:129], v[130:133], v[178:181], v[126:129]
	s_waitcnt lgkmcnt(6)
	v_mfma_f32_16x16x32_bf16 v[126:129], v[134:137], v[182:185], v[126:129]
	v_mfma_f32_16x16x32_bf16 v[122:125], v[138:141], v[178:181], v[122:125]
	s_nop 0
	v_mfma_f32_16x16x32_bf16 v[122:125], v[142:145], v[182:185], v[122:125]
	s_waitcnt lgkmcnt(5)
	v_mfma_f32_16x16x32_bf16 v[110:113], v[130:133], v[186:189], v[110:113]
	s_waitcnt lgkmcnt(4)
	v_mfma_f32_16x16x32_bf16 v[110:113], v[134:137], v[190:193], v[110:113]
	v_mfma_f32_16x16x32_bf16 v[106:109], v[138:141], v[186:189], v[106:109]
	s_nop 0
	v_mfma_f32_16x16x32_bf16 v[106:109], v[142:145], v[190:193], v[106:109]
	s_waitcnt lgkmcnt(3)
	v_mfma_f32_16x16x32_bf16 v[94:97], v[130:133], v[194:197], v[94:97]
	s_waitcnt lgkmcnt(2)
	v_mfma_f32_16x16x32_bf16 v[94:97], v[134:137], v[198:201], v[94:97]
	v_mfma_f32_16x16x32_bf16 v[90:93], v[138:141], v[194:197], v[90:93]
	s_nop 0
	v_mfma_f32_16x16x32_bf16 v[90:93], v[142:145], v[198:201], v[90:93]
	s_waitcnt lgkmcnt(1)
	v_mfma_f32_16x16x32_bf16 v[78:81], v[130:133], v[202:205], v[78:81]
	s_waitcnt lgkmcnt(0)
	v_mfma_f32_16x16x32_bf16 v[78:81], v[134:137], v[206:209], v[78:81]
	v_mfma_f32_16x16x32_bf16 v[74:77], v[138:141], v[202:205], v[74:77]
	s_nop 0
	v_mfma_f32_16x16x32_bf16 v[74:77], v[142:145], v[206:209], v[74:77]
	s_setprio 0
	s_setprio 1
	v_mfma_f32_16x16x32_bf16 v[118:121], v[146:149], v[178:181], v[118:121]
	s_nop 0
	v_mfma_f32_16x16x32_bf16 v[118:121], v[150:153], v[182:185], v[118:121]
	v_mfma_f32_16x16x32_bf16 v[114:117], v[154:157], v[178:181], v[114:117]
	s_nop 0
	v_mfma_f32_16x16x32_bf16 v[114:117], v[158:161], v[182:185], v[114:117]
	v_mfma_f32_16x16x32_bf16 v[102:105], v[146:149], v[186:189], v[102:105]
	s_nop 0
	v_mfma_f32_16x16x32_bf16 v[102:105], v[150:153], v[190:193], v[102:105]
	v_mfma_f32_16x16x32_bf16 v[98:101], v[154:157], v[186:189], v[98:101]
	s_nop 0
	v_mfma_f32_16x16x32_bf16 v[98:101], v[158:161], v[190:193], v[98:101]
	v_mfma_f32_16x16x32_bf16 v[86:89], v[146:149], v[194:197], v[86:89]
	s_nop 0
	v_mfma_f32_16x16x32_bf16 v[86:89], v[150:153], v[198:201], v[86:89]
	v_mfma_f32_16x16x32_bf16 v[82:85], v[154:157], v[194:197], v[82:85]
	s_nop 0
	v_mfma_f32_16x16x32_bf16 v[82:85], v[158:161], v[198:201], v[82:85]
	v_mfma_f32_16x16x32_bf16 v[70:73], v[146:149], v[202:205], v[70:73]
	s_nop 0
	v_mfma_f32_16x16x32_bf16 v[70:73], v[150:153], v[206:209], v[70:73]
	v_mfma_f32_16x16x32_bf16 v[66:69], v[154:157], v[202:205], v[66:69]
	s_nop 0
	v_mfma_f32_16x16x32_bf16 v[66:69], v[158:161], v[206:209], v[66:69]
	s_setprio 0
	s_barrier
; #define LAS __attribute__((address_space(3)))
; #define PG8_STAGE_A(bufoff, soff, voff) do { _Pragma("unroll") for (int _i = 0; _i < 2; ++_i) \
;         __builtin_amdgcn_raw_ptr_buffer_load_lds(rsA, (LAS void*)(lds + (bufoff) + ldsw + _i * 8192), 16, (voff)[_i], (soff), 0, 0); } while (0)
; #define PG8_STAGE_B(bufoff, soff) do { _Pragma("unroll") for (int _i = 0; _i < 2; ++_i) \
;         __builtin_amdgcn_raw_ptr_buffer_load_lds(rsB, (LAS void*)(lds + (bufoff) + ldsw + _i * 8192), 16, voffB[_i], (soff), 0, 0); } while (0)
; #define PG8_LDA(dst, b, h) do { _Pragma("unroll") for (int m = 0; m < 4; ++m) dst[m] = PG8_LD8(lds + PG8_SA(b, h) + aoff + m * 2048); } while (0)
; #define PG8_WAIT_V(n) asm volatile("s_waitcnt vmcnt(" #n ")" ::: "memory")
; #define PG8_WAIT_L(n) asm volatile("s_waitcnt lgkmcnt(" #n ")" ::: "memory")
; #define PG8_BAR __builtin_amdgcn_s_barrier()
; #define PG8_SCHED __builtin_amdgcn_sched_barrier(0)
; template <class Epi, class Sched, bool GATHER, bool ALIGN_EPI, bool SP2, bool FP8>
; __device__ __forceinline__ void gemm_phase(LAS unsigned char* lds, const Gemm g, const Sched& S, const Epi& E) {
;     ...
;             PG8_LDA(At, 1, 1); PG8_STAGE_B(PG8_SB(1, 0), b3); PG8_STAGE_B(PG8_SB(1, 1), b3 + hstep); PG8_STAGE_A(PG8_SA(1, 0), a3, va20);
;             PG8_WAIT_V(8); PG8_WAIT_L(0); PG8_BAR; PG8_MMA(1, 0, At, B0); PG8_MMA(1, 1, At, B1); PG8_BAR; PG8_SCHED;
;     __device__ __forceinline__ void operator()(const f32x4 (&acc)[2][2][4][2], const pg8::Unit& u, const Pre&, int wr, int wc, int fr, int fq) const {
;         const int lane = fr | (fq << 4), rr = lane >> 3, pc = lane & 7;
;         LAS unsigned char* slab = scr + (wr * 4 + wc) * 2048;
;         LAS unsigned char* wp0 = slab + fr * 128 + (((2 * fq) ^ (fr & 7)) << 4); LAS unsigned char* wp1 = slab + fr * 128 + (((2 * fq + 1) ^ (fr & 7)) << 4);
;         const LAS unsigned char* rp0 = slab + rr * 128 + ((pc ^ (rr & 7)) << 4); const LAS unsigned char* rp1 = rp0 + 1024;
;         const size_t base = (size_t)(u.pm * 256 + wr * 64 + rr) * DM + u.pn * 256 + wc * 32 + 4 * pc;
;         f32x4 xa[2][2], xb[2][2];
;     ...
;         EPO_LOAD(xa, 0);
;         EPO_LOAD(xb, 1); __builtin_amdgcn_sched_barrier(0); EPO_DO(xa, 0); __builtin_amdgcn_sched_barrier(0);
	s_mov_b32 m0, s46
	s_or_b32 s82, s81, 0x80
	ds_read_b128 v[178:181], v174 offset:49152
	ds_read_b128 v[182:185], v174 offset:50176
	ds_read_b128 v[186:189], v174 offset:51200
	ds_read_b128 v[190:193], v174 offset:52224
	ds_read_b128 v[194:197], v174 offset:53248
	ds_read_b128 v[198:201], v174 offset:54272
	ds_read_b128 v[202:205], v174 offset:55296
	ds_read_b128 v[206:209], v174 offset:56320
	buffer_load_dwordx4 v1, s[8:11], s82 offen lds
	s_mov_b32 m0, s47
	s_add_i32 s81, s81, 0x80080
	buffer_load_dwordx4 v163, s[8:11], s82 offen lds
	s_mov_b32 m0, s50
	s_nop 0
	buffer_load_dwordx4 v1, s[8:11], s81 offen lds
	s_mov_b32 m0, s51
	s_nop 0
	buffer_load_dwordx4 v163, s[8:11], s81 offen lds
	s_mov_b32 m0, s48
	s_nop 0
	buffer_load_dwordx4 v168, s[4:7], s80 offen lds
	s_mov_b32 m0, s49
	s_nop 0
	buffer_load_dwordx4 v169, s[4:7], s80 offen lds
	s_waitcnt vmcnt(8)
	s_waitcnt lgkmcnt(0)
	s_barrier
	s_setprio 1
	s_waitcnt lgkmcnt(7)
	v_mfma_f32_16x16x32_bf16 v[62:65], v[130:133], v[178:181], v[62:65]
	s_waitcnt lgkmcnt(6)
	v_mfma_f32_16x16x32_bf16 v[62:65], v[134:137], v[182:185], v[62:65]
	v_mfma_f32_16x16x32_bf16 v[58:61], v[138:141], v[178:181], v[58:61]
	s_nop 0
	v_mfma_f32_16x16x32_bf16 v[58:61], v[142:145], v[182:185], v[58:61]
	s_waitcnt lgkmcnt(5)
	v_mfma_f32_16x16x32_bf16 v[46:49], v[130:133], v[186:189], v[46:49]
	s_waitcnt lgkmcnt(4)
	v_mfma_f32_16x16x32_bf16 v[46:49], v[134:137], v[190:193], v[46:49]
	v_mfma_f32_16x16x32_bf16 v[42:45], v[138:141], v[186:189], v[42:45]
	s_nop 0
	v_mfma_f32_16x16x32_bf16 v[42:45], v[142:145], v[190:193], v[42:45]
	s_waitcnt lgkmcnt(3)
	v_mfma_f32_16x16x32_bf16 v[30:33], v[130:133], v[194:197], v[30:33]
	s_waitcnt lgkmcnt(2)
	v_mfma_f32_16x16x32_bf16 v[30:33], v[134:137], v[198:201], v[30:33]
	v_mfma_f32_16x16x32_bf16 v[26:29], v[138:141], v[194:197], v[26:29]
	s_nop 0
	v_mfma_f32_16x16x32_bf16 v[26:29], v[142:145], v[198:201], v[26:29]
	s_waitcnt lgkmcnt(1)
	v_mfma_f32_16x16x32_bf16 v[14:17], v[130:133], v[202:205], v[14:17]
	s_waitcnt lgkmcnt(0)
	v_mfma_f32_16x16x32_bf16 v[14:17], v[134:137], v[206:209], v[14:17]
	v_mfma_f32_16x16x32_bf16 v[10:13], v[138:141], v[202:205], v[10:13]
	s_nop 0
	v_mfma_f32_16x16x32_bf16 v[10:13], v[142:145], v[206:209], v[10:13]
	s_setprio 0
	s_setprio 1
	v_mfma_f32_16x16x32_bf16 v[54:57], v[146:149], v[178:181], v[54:57]
	s_nop 0
	v_mfma_f32_16x16x32_bf16 v[54:57], v[150:153], v[182:185], v[54:57]
	v_mfma_f32_16x16x32_bf16 v[50:53], v[154:157], v[178:181], v[50:53]
	s_nop 0
	v_mfma_f32_16x16x32_bf16 v[50:53], v[158:161], v[182:185], v[50:53]
	v_mfma_f32_16x16x32_bf16 v[38:41], v[146:149], v[186:189], v[38:41]
	s_nop 0
	v_mfma_f32_16x16x32_bf16 v[38:41], v[150:153], v[190:193], v[38:41]
	v_mfma_f32_16x16x32_bf16 v[34:37], v[154:157], v[186:189], v[34:37]
	s_nop 0
	v_mfma_f32_16x16x32_bf16 v[34:37], v[158:161], v[190:193], v[34:37]
	v_mfma_f32_16x16x32_bf16 v[22:25], v[146:149], v[194:197], v[22:25]
	s_nop 0
	v_mfma_f32_16x16x32_bf16 v[22:25], v[150:153], v[198:201], v[22:25]
	v_mfma_f32_16x16x32_bf16 v[18:21], v[154:157], v[194:197], v[18:21]
	s_nop 0
	v_mfma_f32_16x16x32_bf16 v[18:21], v[158:161], v[198:201], v[18:21]
	v_mfma_f32_16x16x32_bf16 v[6:9], v[146:149], v[202:205], v[6:9]
	s_nop 0
	v_mfma_f32_16x16x32_bf16 v[6:9], v[150:153], v[206:209], v[6:9]
	v_mfma_f32_16x16x32_bf16 v[2:5], v[154:157], v[202:205], v[2:5]
	s_nop 0
	v_mfma_f32_16x16x32_bf16 v[2:5], v[158:161], v[206:209], v[2:5]
	s_setprio 0
	s_barrier
	s_add_i32 s79, s79, 2
	s_addk_i32 s77, 0x100
	s_addk_i32 s78, 0x100
	s_cmp_gt_u32 s79, 29
	s_cbranch_scc0 .LBB0_708
	s_mov_b32 s10, 0
	s_mov_b32 s11, 0
	s_nop 15
	s_nop 3
	v_mov_b32_e32 v154, v0
	v_readlane_b32 s80, v245, 21
	v_readfirstlane_b32 s10, v154
	s_ashr_i32 s75, s10, 8
	s_bfe_u32 s76, s10, 0x20006
	s_lshl_b32 s10, s74, 8
	s_lshl_b32 s11, s75, 6
	v_bfe_u32 v155, v154, 3, 3
	s_add_i32 s11, s11, s10
	v_or_b32_e32 v130, s11, v155
	v_ashrrev_i32_e32 v131, 31, v130
	s_lshl_b32 s10, s33, 8
	v_and_b32_e32 v177, 7, v154
	v_lshlrev_b64 v[130:131], 11, v[130:131]
	s_ashr_i32 s11, s10, 31
	v_lshl_add_u64 v[160:161], v[130:131], 0, s[10:11]
	s_lshl_b32 s10, s76, 5
	v_lshlrev_b32_e32 v130, 2, v177
	v_or3_b32 v160, v160, s10, v130
	v_lshlrev_b64 v[186:187], 2, v[160:161]
	v_readlane_b32 s81, v245, 22
	s_lshl_b32 s10, s75, 13
	s_lshl_b32 s11, s76, 11
	v_lshl_add_u64 v[150:151], s[80:81], 0, v[186:187]
	v_add_co_u32_e32 v130, vcc, s45, v150
	s_add_i32 s10, s10, 0
	s_nop 0
	v_addc_co_u32_e32 v131, vcc, 0, v151, vcc
	v_add_co_u32_e32 v132, vcc, s7, v150
	global_load_dwordx4 v[146:149], v[150:151], off nt
	global_load_dwordx4 v[156:159], v[150:151], off offset:512 nt
	global_load_dwordx4 v[178:181], v[130:131], off nt
	global_load_dwordx4 v[182:185], v[130:131], off offset:512 nt
	v_addc_co_u32_e32 v133, vcc, 0, v151, vcc
	v_lshl_add_u64 v[130:131], v[150:151], 0, s[16:17]
	v_add_co_u32_e32 v152, vcc, s57, v150
	s_add_i32 s10, s10, s11
	s_nop 0
	v_addc_co_u32_e32 v153, vcc, 0, v151, vcc
	global_load_dwordx4 v[142:145], v[132:133], off nt
	global_load_dwordx4 v[134:137], v[130:131], off offset:512 nt
	global_load_dwordx4 v[138:141], v[152:153], off nt
	s_nop 0
	global_load_dwordx4 v[130:133], v[152:153], off offset:512 nt
	v_lshrrev_b32_e32 v152, 3, v154
	v_lshlrev_b32_e32 v153, 7, v154
	s_add_i32 s10, s10, 0x20000
	v_and_b32_e32 v153, 0x780, v153
	v_and_b32_e32 v188, 6, v152
	v_bitop3_b32 v189, v152, v177, 6 bitop3:0x6c
	v_bitop3_b32 v152, v152, v154, 7 bitop3:0x28
	v_readlane_b32 s82, v245, 23
	v_readlane_b32 s83, v245, 24
	v_readlane_b32 s94, v245, 35
	v_bitop3_b32 v177, v188, v177, 1 bitop3:0x36
	v_lshlrev_b32_e32 v155, 7, v155
	v_lshlrev_b32_e32 v152, 4, v152
	v_add_u32_e32 v154, s10, v153
	v_readlane_b32 s84, v245, 25
	v_readlane_b32 s85, v245, 26
	v_readlane_b32 s86, v245, 27
	v_readlane_b32 s87, v245, 28
	v_readlane_b32 s88, v245, 29
	v_readlane_b32 s89, v245, 30
	v_readlane_b32 s90, v245, 31
	v_readlane_b32 s91, v245, 32
	v_readlane_b32 s92, v245, 33
	v_readlane_b32 s93, v245, 34
	v_readlane_b32 s95, v245, 36
	v_add3_u32 v152, s10, v155, v152
	v_lshl_add_u32 v153, v177, 4, v154
	v_lshl_add_u32 v154, v189, 4, v154
	ds_write_b128 v154, v[126:129]
	ds_write_b128 v153, v[122:125]
	ds_read_b128 v[122:125], v152
	ds_read_b128 v[126:129], v152 offset:1024
	v_mov_b32_e32 v155, 0
	s_movk_i32 s10, 0x4000
	s_waitcnt vmcnt(7) lgkmcnt(1)
; #define EPO_LOAD(dst, g) do { const size_t off_ = base + (size_t)(((g) >> 2) * 128 + ((g) & 3) * 16) * DM; \
;         _Pragma("unroll") for (int bj_ = 0; bj_ < 2; ++bj_) { dst[bj_][0] = *(const f32x4*)(X + off_ + bj_ * 128); dst[bj_][1] = *(const f32x4*)(X + off_ + bj_ * 128 + (size_t)8 * DM); } } while (0)
;     __device__ __forceinline__ void operator()(const f32x4 (&acc)[2][2][4][2], const pg8::Unit& u, const Pre&, int wr, int wc, int fr, int fq) const {
;     ...
;         EPO_LOAD(xa, 0);
;         EPO_LOAD(xb, 1); __builtin_amdgcn_sched_barrier(0); EPO_DO(xa, 0); __builtin_amdgcn_sched_barrier(0);
;         EPO_LOAD(xa, 2); __builtin_amdgcn_sched_barrier(0); EPO_DO(xb, 1); __builtin_amdgcn_sched_barrier(0);
;         EPO_LOAD(xb, 3); __builtin_amdgcn_sched_barrier(0); EPO_DO(xa, 2); __builtin_amdgcn_sched_barrier(0);
	v_pk_add_f32 v[122:123], v[146:147], v[122:123]
	s_nop 0
	v_cvt_pk_fp8_f32 v155, v122, v123
	v_pk_add_f32 v[124:125], v[148:149], v[124:125]
	v_lshl_add_u64 v[148:149], s[12:13], 0, v[186:187]
	s_waitcnt vmcnt(5) lgkmcnt(0)
	v_pk_add_f32 v[126:127], v[178:179], v[126:127]
	global_store_dwordx4 v[148:149], v[122:125], off
	v_cvt_pk_fp8_f32 v155, v124, v125 op_sel:[0,0,1]
	v_pk_add_f32 v[128:129], v[180:181], v[128:129]
	v_mov_b32_e32 v124, 0
	v_cvt_pk_fp8_f32 v124, v126, v127
	v_add_co_u32_e32 v178, vcc, s45, v148
	v_lshl_add_u64 v[146:147], s[14:15], 0, v[160:161]
	v_cvt_pk_fp8_f32 v124, v128, v129 op_sel:[0,0,1]
	v_addc_co_u32_e32 v179, vcc, 0, v149, vcc
	v_add_co_u32_e32 v122, vcc, s10, v146
	global_store_dwordx4 v[178:179], v[126:129], off
	s_nop 0
	v_addc_co_u32_e32 v123, vcc, 0, v147, vcc
	global_store_dword v[146:147], v155, off
	global_store_dword v[122:123], v124, off
	ds_write_b128 v154, v[118:121]
	ds_write_b128 v153, v[114:117]
	ds_read_b128 v[114:117], v152
	ds_read_b128 v[118:121], v152 offset:1024
	v_mov_b32_e32 v124, 0
	s_waitcnt lgkmcnt(1)
	v_pk_add_f32 v[116:117], v[158:159], v[116:117]
	v_pk_add_f32 v[114:115], v[156:157], v[114:115]
	s_waitcnt vmcnt(8) lgkmcnt(0)
	v_pk_add_f32 v[120:121], v[184:185], v[120:121]
	v_pk_add_f32 v[118:119], v[182:183], v[118:119]
	global_store_dwordx4 v[148:149], v[114:117], off offset:512
	global_store_dwordx4 v[178:179], v[118:121], off offset:512
	v_cvt_pk_fp8_f32 v124, v114, v115
	v_mov_b32_e32 v114, 0
	v_cvt_pk_fp8_f32 v114, v118, v119
	v_cvt_pk_fp8_f32 v124, v116, v117 op_sel:[0,0,1]
	v_cvt_pk_fp8_f32 v114, v120, v121 op_sel:[0,0,1]
	global_store_dword v[146:147], v124, off offset:128
	global_store_dword v[122:123], v114, off offset:128
	v_add_co_u32_e32 v116, vcc, s58, v150
	v_lshl_add_u64 v[114:115], v[150:151], 0, s[18:19]
	s_nop 0
	v_addc_co_u32_e32 v117, vcc, 0, v151, vcc
	v_add_co_u32_e32 v156, vcc, s59, v150
	s_nop 1
	v_addc_co_u32_e32 v157, vcc, 0, v151, vcc
	global_load_dwordx4 v[126:129], v[116:117], off nt
	global_load_dwordx4 v[118:121], v[114:115], off offset:512 nt
	global_load_dwordx4 v[122:125], v[156:157], off nt
	s_nop 0
	global_load_dwordx4 v[114:117], v[156:157], off offset:512 nt
	ds_write_b128 v154, v[110:113]
	ds_write_b128 v153, v[106:109]
	ds_read_b128 v[106:109], v152
	ds_read_b128 v[110:113], v152 offset:1024
	s_mov_b64 s[10:11], 0x8000
	s_waitcnt vmcnt(15) lgkmcnt(1)
	v_pk_add_f32 v[106:107], v[142:143], v[106:107]
	v_mov_b32_e32 v142, 0
	v_cvt_pk_fp8_f32 v142, v106, v107
	s_waitcnt vmcnt(13) lgkmcnt(0)
	v_pk_add_f32 v[112:113], v[140:141], v[112:113]
	v_add_co_u32_e32 v140, vcc, s7, v148
	v_pk_add_f32 v[108:109], v[144:145], v[108:109]
	s_nop 0
	v_addc_co_u32_e32 v141, vcc, 0, v149, vcc
	global_store_dwordx4 v[140:141], v[106:109], off
	v_add_co_u32_e32 v140, vcc, s57, v148
	v_cvt_pk_fp8_f32 v142, v108, v109 op_sel:[0,0,1]
	s_nop 0
	v_addc_co_u32_e32 v141, vcc, 0, v149, vcc
	v_lshl_add_u64 v[106:107], v[146:147], 0, s[10:11]
	s_mov_b32 s10, 0x8000
	v_add_co_u32_e32 v108, vcc, s10, v146
	v_pk_add_f32 v[110:111], v[138:139], v[110:111]
	s_nop 0
	v_addc_co_u32_e32 v109, vcc, 0, v147, vcc
	global_store_dwordx4 v[140:141], v[110:113], off
	global_store_dword v[108:109], v142, off
	v_mov_b32_e32 v142, 0
	v_cvt_pk_fp8_f32 v142, v110, v111
	s_mov_b32 s10, 0xc000
	v_add_co_u32_e32 v108, vcc, s10, v146
	v_cvt_pk_fp8_f32 v142, v112, v113 op_sel:[0,0,1]
	s_nop 0
	v_addc_co_u32_e32 v109, vcc, 0, v147, vcc
	v_lshl_add_u64 v[138:139], v[148:149], 0, s[16:17]
	global_store_dword v[108:109], v142, off
	ds_write_b128 v154, v[102:105]
	ds_write_b128 v153, v[98:101]
	ds_read_b128 v[98:101], v152
	ds_read_b128 v[102:105], v152 offset:1024
	v_mov_b32_e32 v110, 0
	s_waitcnt lgkmcnt(1)
	v_pk_add_f32 v[100:101], v[136:137], v[100:101]
	v_pk_add_f32 v[98:99], v[134:135], v[98:99]
	s_waitcnt vmcnt(16) lgkmcnt(0)
	v_pk_add_f32 v[104:105], v[132:133], v[104:105]
	v_pk_add_f32 v[102:103], v[130:131], v[102:103]
	global_store_dwordx4 v[138:139], v[98:101], off offset:512
	global_store_dwordx4 v[140:141], v[102:105], off offset:512
	v_cvt_pk_fp8_f32 v110, v98, v99
	v_mov_b32_e32 v98, 0
	v_cvt_pk_fp8_f32 v98, v102, v103
	v_cvt_pk_fp8_f32 v110, v100, v101 op_sel:[0,0,1]
	v_cvt_pk_fp8_f32 v98, v104, v105 op_sel:[0,0,1]
	global_store_dword v[106:107], v110, off offset:128
	global_store_dword v[108:109], v98, off offset:128
	v_add_co_u32_e32 v100, vcc, s60, v150
	v_lshl_add_u64 v[98:99], v[150:151], 0, s[20:21]
	s_nop 0
	v_addc_co_u32_e32 v101, vcc, 0, v151, vcc
	v_add_co_u32_e32 v130, vcc, s61, v150
	s_nop 1
	v_addc_co_u32_e32 v131, vcc, 0, v151, vcc
	global_load_dwordx4 v[110:113], v[100:101], off nt
	global_load_dwordx4 v[102:105], v[98:99], off offset:512 nt
	global_load_dwordx4 v[106:109], v[130:131], off nt
	s_nop 0
	global_load_dwordx4 v[98:101], v[130:131], off offset:512 nt
	ds_write_b128 v154, v[94:97]
	ds_write_b128 v153, v[90:93]
	ds_read_b128 v[90:93], v152
	ds_read_b128 v[94:97], v152 offset:1024
	s_mov_b64 s[10:11], 0x10000
	s_waitcnt vmcnt(15) lgkmcnt(1)
	v_pk_add_f32 v[90:91], v[126:127], v[90:91]
	v_mov_b32_e32 v126, 0
	v_cvt_pk_fp8_f32 v126, v90, v91
	s_waitcnt vmcnt(13) lgkmcnt(0)
; #define EPO_LOAD(dst, g) do { const size_t off_ = base + (size_t)(((g) >> 2) * 128 + ((g) & 3) * 16) * DM; \
;         _Pragma("unroll") for (int bj_ = 0; bj_ < 2; ++bj_) { dst[bj_][0] = *(const f32x4*)(X + off_ + bj_ * 128); dst[bj_][1] = *(const f32x4*)(X + off_ + bj_ * 128 + (size_t)8 * DM); } } while (0)
;     __device__ __forceinline__ void operator()(const f32x4 (&acc)[2][2][4][2], const pg8::Unit& u, const Pre&, int wr, int wc, int fr, int fq) const {
;     ...
;         EPO_LOAD(xa, 0);
;         EPO_LOAD(xb, 1); __builtin_amdgcn_sched_barrier(0); EPO_DO(xa, 0); __builtin_amdgcn_sched_barrier(0);
;         EPO_LOAD(xa, 2); __builtin_amdgcn_sched_barrier(0); EPO_DO(xb, 1); __builtin_amdgcn_sched_barrier(0);
;         EPO_LOAD(xb, 3); __builtin_amdgcn_sched_barrier(0); EPO_DO(xa, 2); __builtin_amdgcn_sched_barrier(0);
;         EPO_LOAD(xa, 4); __builtin_amdgcn_sched_barrier(0); EPO_DO(xb, 3); __builtin_amdgcn_sched_barrier(0);
;         EPO_LOAD(xb, 5); __builtin_amdgcn_sched_barrier(0); EPO_DO(xa, 4); __builtin_amdgcn_sched_barrier(0);
	v_pk_add_f32 v[96:97], v[124:125], v[96:97]
	v_add_co_u32_e32 v124, vcc, s58, v148
	v_pk_add_f32 v[92:93], v[128:129], v[92:93]
	s_nop 0
	v_addc_co_u32_e32 v125, vcc, 0, v149, vcc
	global_store_dwordx4 v[124:125], v[90:93], off
	v_add_co_u32_e32 v124, vcc, s59, v148
	v_cvt_pk_fp8_f32 v126, v92, v93 op_sel:[0,0,1]
	s_nop 0
	v_addc_co_u32_e32 v125, vcc, 0, v149, vcc
	v_add_co_u32_e32 v92, vcc, s45, v146
	v_pk_add_f32 v[94:95], v[122:123], v[94:95]
	s_nop 0
	v_addc_co_u32_e32 v93, vcc, 0, v147, vcc
	global_store_dwordx4 v[124:125], v[94:97], off
	global_store_dword v[92:93], v126, off
	v_mov_b32_e32 v126, 0
	v_cvt_pk_fp8_f32 v126, v94, v95
	v_lshl_add_u64 v[90:91], v[146:147], 0, s[10:11]
	s_mov_b32 s10, 0x14000
	v_add_co_u32_e32 v92, vcc, s10, v146
	v_cvt_pk_fp8_f32 v126, v96, v97 op_sel:[0,0,1]
	s_nop 0
	v_addc_co_u32_e32 v93, vcc, 0, v147, vcc
	v_lshl_add_u64 v[122:123], v[148:149], 0, s[18:19]
	global_store_dword v[92:93], v126, off
	ds_write_b128 v154, v[86:89]
	ds_write_b128 v153, v[82:85]
	ds_read_b128 v[82:85], v152
	ds_read_b128 v[86:89], v152 offset:1024
	v_mov_b32_e32 v94, 0
	s_waitcnt lgkmcnt(1)
	v_pk_add_f32 v[84:85], v[120:121], v[84:85]
	v_pk_add_f32 v[82:83], v[118:119], v[82:83]
	s_waitcnt vmcnt(16) lgkmcnt(0)
	v_pk_add_f32 v[88:89], v[116:117], v[88:89]
	v_pk_add_f32 v[86:87], v[114:115], v[86:87]
	global_store_dwordx4 v[122:123], v[82:85], off offset:512
	global_store_dwordx4 v[124:125], v[86:89], off offset:512
	v_cvt_pk_fp8_f32 v94, v82, v83
	v_mov_b32_e32 v82, 0
	v_cvt_pk_fp8_f32 v82, v86, v87
	v_cvt_pk_fp8_f32 v94, v84, v85 op_sel:[0,0,1]
	v_cvt_pk_fp8_f32 v82, v88, v89 op_sel:[0,0,1]
	global_store_dword v[90:91], v94, off offset:128
	global_store_dword v[92:93], v82, off offset:128
	v_add_co_u32_e32 v84, vcc, s62, v150
	v_lshl_add_u64 v[82:83], v[150:151], 0, s[22:23]
	s_nop 0
	v_addc_co_u32_e32 v85, vcc, 0, v151, vcc
	v_add_co_u32_e32 v114, vcc, s63, v150
	s_nop 1
	v_addc_co_u32_e32 v115, vcc, 0, v151, vcc
	global_load_dwordx4 v[94:97], v[84:85], off nt
	global_load_dwordx4 v[86:89], v[82:83], off offset:512 nt
	global_load_dwordx4 v[90:93], v[114:115], off nt
	s_nop 0
	global_load_dwordx4 v[82:85], v[114:115], off offset:512 nt
	ds_write_b128 v154, v[78:81]
	ds_write_b128 v153, v[74:77]
	ds_read_b128 v[74:77], v152
	ds_read_b128 v[78:81], v152 offset:1024
	s_mov_b64 s[10:11], 0x18000
	s_waitcnt vmcnt(15) lgkmcnt(1)
	v_pk_add_f32 v[74:75], v[110:111], v[74:75]
	v_mov_b32_e32 v110, 0
	v_cvt_pk_fp8_f32 v110, v74, v75
	s_waitcnt vmcnt(13) lgkmcnt(0)
	v_pk_add_f32 v[80:81], v[108:109], v[80:81]
	v_add_co_u32_e32 v108, vcc, s60, v148
	v_pk_add_f32 v[76:77], v[112:113], v[76:77]
	s_nop 0
	v_addc_co_u32_e32 v109, vcc, 0, v149, vcc
	global_store_dwordx4 v[108:109], v[74:77], off
	v_add_co_u32_e32 v108, vcc, s61, v148
	v_cvt_pk_fp8_f32 v110, v76, v77 op_sel:[0,0,1]
	s_nop 0
	v_addc_co_u32_e32 v109, vcc, 0, v149, vcc
	v_lshl_add_u64 v[74:75], v[146:147], 0, s[10:11]
	s_mov_b32 s10, 0x18000
	v_add_co_u32_e32 v76, vcc, s10, v146
	v_pk_add_f32 v[78:79], v[106:107], v[78:79]
	s_nop 0
	v_addc_co_u32_e32 v77, vcc, 0, v147, vcc
	global_store_dwordx4 v[108:109], v[78:81], off
	global_store_dword v[76:77], v110, off
	v_mov_b32_e32 v110, 0
	v_cvt_pk_fp8_f32 v110, v78, v79
	s_mov_b32 s10, 0x1c000
	v_add_co_u32_e32 v76, vcc, s10, v146
	v_cvt_pk_fp8_f32 v110, v80, v81 op_sel:[0,0,1]
	s_nop 0
	v_addc_co_u32_e32 v77, vcc, 0, v147, vcc
	v_lshl_add_u64 v[106:107], v[148:149], 0, s[20:21]
	global_store_dword v[76:77], v110, off
	ds_write_b128 v154, v[70:73]
	ds_write_b128 v153, v[66:69]
	ds_read_b128 v[66:69], v152
	ds_read_b128 v[70:73], v152 offset:1024
	v_mov_b32_e32 v78, 0
	s_waitcnt lgkmcnt(1)
	v_pk_add_f32 v[68:69], v[104:105], v[68:69]
	v_pk_add_f32 v[66:67], v[102:103], v[66:67]
	s_waitcnt vmcnt(16) lgkmcnt(0)
	v_pk_add_f32 v[72:73], v[100:101], v[72:73]
	v_pk_add_f32 v[70:71], v[98:99], v[70:71]
	global_store_dwordx4 v[106:107], v[66:69], off offset:512
	global_store_dwordx4 v[108:109], v[70:73], off offset:512
	v_cvt_pk_fp8_f32 v78, v66, v67
	v_mov_b32_e32 v66, 0
	v_cvt_pk_fp8_f32 v66, v70, v71
	v_cvt_pk_fp8_f32 v78, v68, v69 op_sel:[0,0,1]
	v_cvt_pk_fp8_f32 v66, v72, v73 op_sel:[0,0,1]
	global_store_dword v[74:75], v78, off offset:128
	global_store_dword v[76:77], v66, off offset:128
	v_add_co_u32_e32 v68, vcc, s64, v150
	v_lshl_add_u64 v[66:67], v[150:151], 0, s[24:25]
	s_nop 0
	v_addc_co_u32_e32 v69, vcc, 0, v151, vcc
	v_add_co_u32_e32 v98, vcc, s65, v150
	s_nop 1
	v_addc_co_u32_e32 v99, vcc, 0, v151, vcc
	global_load_dwordx4 v[78:81], v[68:69], off nt
	global_load_dwordx4 v[70:73], v[66:67], off offset:512 nt
	global_load_dwordx4 v[74:77], v[98:99], off nt
	s_nop 0
	global_load_dwordx4 v[66:69], v[98:99], off offset:512 nt
	ds_write_b128 v154, v[62:65]
	ds_write_b128 v153, v[58:61]
	ds_read_b128 v[58:61], v152
	ds_read_b128 v[62:65], v152 offset:1024
	s_mov_b32 s10, 0x44000
	s_waitcnt vmcnt(15) lgkmcnt(1)
	v_pk_add_f32 v[58:59], v[94:95], v[58:59]
	v_mov_b32_e32 v94, 0
	v_cvt_pk_fp8_f32 v94, v58, v59
	s_waitcnt vmcnt(13) lgkmcnt(0)
	v_pk_add_f32 v[64:65], v[92:93], v[64:65]
	v_add_co_u32_e32 v92, vcc, s62, v148
	v_pk_add_f32 v[60:61], v[96:97], v[60:61]
	s_nop 0
	v_addc_co_u32_e32 v93, vcc, 0, v149, vcc
	global_store_dwordx4 v[92:93], v[58:61], off
	v_add_co_u32_e32 v92, vcc, s63, v148
	v_cvt_pk_fp8_f32 v94, v60, v61 op_sel:[0,0,1]
	s_nop 0
	v_addc_co_u32_e32 v93, vcc, 0, v149, vcc
	v_add_co_u32_e32 v60, vcc, s58, v146
	v_pk_add_f32 v[62:63], v[90:91], v[62:63]
	s_nop 0
	v_addc_co_u32_e32 v61, vcc, 0, v147, vcc
	global_store_dwordx4 v[92:93], v[62:65], off
	global_store_dword v[60:61], v94, off
	v_mov_b32_e32 v94, 0
	v_cvt_pk_fp8_f32 v94, v62, v63
	v_add_co_u32_e32 v60, vcc, s10, v146
	v_lshl_add_u64 v[90:91], v[148:149], 0, s[22:23]
	v_cvt_pk_fp8_f32 v94, v64, v65 op_sel:[0,0,1]
	v_addc_co_u32_e32 v61, vcc, 0, v147, vcc
	v_mov_b32_e32 v62, 0
	global_store_dword v[60:61], v94, off
	ds_write_b128 v154, v[54:57]
	ds_write_b128 v153, v[50:53]
	ds_read_b128 v[50:53], v152
	ds_read_b128 v[54:57], v152 offset:1024
	v_lshl_add_u64 v[58:59], v[146:147], 0, s[18:19]
	s_waitcnt lgkmcnt(1)
; #define EPO_LOAD(dst, g) do { const size_t off_ = base + (size_t)(((g) >> 2) * 128 + ((g) & 3) * 16) * DM; \
;         _Pragma("unroll") for (int bj_ = 0; bj_ < 2; ++bj_) { dst[bj_][0] = *(const f32x4*)(X + off_ + bj_ * 128); dst[bj_][1] = *(const f32x4*)(X + off_ + bj_ * 128 + (size_t)8 * DM); } } while (0)
;     __device__ __forceinline__ void operator()(const f32x4 (&acc)[2][2][4][2], const pg8::Unit& u, const Pre&, int wr, int wc, int fr, int fq) const {
;     ...
;         EPO_LOAD(xa, 0);
;         EPO_LOAD(xb, 1); __builtin_amdgcn_sched_barrier(0); EPO_DO(xa, 0); __builtin_amdgcn_sched_barrier(0);
;         EPO_LOAD(xa, 2); __builtin_amdgcn_sched_barrier(0); EPO_DO(xb, 1); __builtin_amdgcn_sched_barrier(0);
;         EPO_LOAD(xb, 3); __builtin_amdgcn_sched_barrier(0); EPO_DO(xa, 2); __builtin_amdgcn_sched_barrier(0);
;         EPO_LOAD(xa, 4); __builtin_amdgcn_sched_barrier(0); EPO_DO(xb, 3); __builtin_amdgcn_sched_barrier(0);
;         EPO_LOAD(xb, 5); __builtin_amdgcn_sched_barrier(0); EPO_DO(xa, 4); __builtin_amdgcn_sched_barrier(0);
;         EPO_LOAD(xa, 6); __builtin_amdgcn_sched_barrier(0); EPO_DO(xb, 5); __builtin_amdgcn_sched_barrier(0);
	v_pk_add_f32 v[52:53], v[88:89], v[52:53]
	v_pk_add_f32 v[50:51], v[86:87], v[50:51]
	s_waitcnt vmcnt(16) lgkmcnt(0)
	v_pk_add_f32 v[56:57], v[84:85], v[56:57]
	v_pk_add_f32 v[54:55], v[82:83], v[54:55]
	global_store_dwordx4 v[90:91], v[50:53], off offset:512
	global_store_dwordx4 v[92:93], v[54:57], off offset:512
	v_cvt_pk_fp8_f32 v62, v50, v51
	v_mov_b32_e32 v50, 0
	v_cvt_pk_fp8_f32 v50, v54, v55
	v_cvt_pk_fp8_f32 v62, v52, v53 op_sel:[0,0,1]
	v_cvt_pk_fp8_f32 v50, v56, v57 op_sel:[0,0,1]
	global_store_dword v[58:59], v62, off offset:128
	global_store_dword v[60:61], v50, off offset:128
	v_add_co_u32_e32 v52, vcc, s66, v150
	v_lshl_add_u64 v[50:51], v[150:151], 0, s[26:27]
	s_nop 0
	v_addc_co_u32_e32 v53, vcc, 0, v151, vcc
	v_add_co_u32_e32 v82, vcc, s67, v150
	s_nop 1
	v_addc_co_u32_e32 v83, vcc, 0, v151, vcc
	global_load_dwordx4 v[62:65], v[52:53], off nt
	global_load_dwordx4 v[54:57], v[50:51], off offset:512 nt
	global_load_dwordx4 v[58:61], v[82:83], off nt
	s_nop 0
	global_load_dwordx4 v[50:53], v[82:83], off offset:512 nt
	ds_write_b128 v154, v[46:49]
	ds_write_b128 v153, v[42:45]
	ds_read_b128 v[42:45], v152
	ds_read_b128 v[46:49], v152 offset:1024
	s_mov_b64 s[10:11], 0x48000
	s_waitcnt vmcnt(15) lgkmcnt(1)
	v_pk_add_f32 v[42:43], v[78:79], v[42:43]
	v_mov_b32_e32 v78, 0
	v_cvt_pk_fp8_f32 v78, v42, v43
	s_waitcnt vmcnt(13) lgkmcnt(0)
	v_pk_add_f32 v[48:49], v[76:77], v[48:49]
	v_add_co_u32_e32 v76, vcc, s64, v148
	v_pk_add_f32 v[44:45], v[80:81], v[44:45]
	s_nop 0
	v_addc_co_u32_e32 v77, vcc, 0, v149, vcc
	global_store_dwordx4 v[76:77], v[42:45], off
	v_add_co_u32_e32 v76, vcc, s65, v148
	v_cvt_pk_fp8_f32 v78, v44, v45 op_sel:[0,0,1]
	s_nop 0
	v_addc_co_u32_e32 v77, vcc, 0, v149, vcc
	v_lshl_add_u64 v[42:43], v[146:147], 0, s[10:11]
	s_mov_b32 s10, 0x48000
	v_add_co_u32_e32 v44, vcc, s10, v146
	v_pk_add_f32 v[46:47], v[74:75], v[46:47]
	s_nop 0
	v_addc_co_u32_e32 v45, vcc, 0, v147, vcc
	global_store_dwordx4 v[76:77], v[46:49], off
	global_store_dword v[44:45], v78, off
	v_mov_b32_e32 v78, 0
	v_cvt_pk_fp8_f32 v78, v46, v47
	s_mov_b32 s10, 0x4c000
	v_add_co_u32_e32 v44, vcc, s10, v146
	v_cvt_pk_fp8_f32 v78, v48, v49 op_sel:[0,0,1]
	s_nop 0
	v_addc_co_u32_e32 v45, vcc, 0, v147, vcc
	v_lshl_add_u64 v[74:75], v[148:149], 0, s[24:25]
	global_store_dword v[44:45], v78, off
	ds_write_b128 v154, v[38:41]
	ds_write_b128 v153, v[34:37]
	ds_read_b128 v[34:37], v152
	ds_read_b128 v[38:41], v152 offset:1024
	v_mov_b32_e32 v46, 0
	s_waitcnt lgkmcnt(1)
	v_pk_add_f32 v[36:37], v[72:73], v[36:37]
	v_pk_add_f32 v[34:35], v[70:71], v[34:35]
	s_waitcnt vmcnt(16) lgkmcnt(0)
	v_pk_add_f32 v[40:41], v[68:69], v[40:41]
	v_pk_add_f32 v[38:39], v[66:67], v[38:39]
	global_store_dwordx4 v[74:75], v[34:37], off offset:512
	global_store_dwordx4 v[76:77], v[38:41], off offset:512
	v_cvt_pk_fp8_f32 v46, v34, v35
	v_mov_b32_e32 v34, 0
	v_cvt_pk_fp8_f32 v34, v38, v39
	v_cvt_pk_fp8_f32 v46, v36, v37 op_sel:[0,0,1]
	v_cvt_pk_fp8_f32 v34, v40, v41 op_sel:[0,0,1]
	global_store_dword v[42:43], v46, off offset:128
	global_store_dword v[44:45], v34, off offset:128
	v_add_co_u32_e32 v36, vcc, s68, v150
	v_lshl_add_u64 v[34:35], v[150:151], 0, s[28:29]
	s_nop 0
	v_addc_co_u32_e32 v37, vcc, 0, v151, vcc
	v_add_co_u32_e32 v66, vcc, s69, v150
	s_nop 1
	v_addc_co_u32_e32 v67, vcc, 0, v151, vcc
	global_load_dwordx4 v[46:49], v[36:37], off nt
	global_load_dwordx4 v[38:41], v[34:35], off offset:512 nt
	global_load_dwordx4 v[42:45], v[66:67], off nt
	s_nop 0
	global_load_dwordx4 v[34:37], v[66:67], off offset:512 nt
	ds_write_b128 v154, v[30:33]
	ds_write_b128 v153, v[26:29]
	ds_read_b128 v[26:29], v152
	ds_read_b128 v[30:33], v152 offset:1024
	s_mov_b64 s[10:11], 0x50000
	s_waitcnt vmcnt(15) lgkmcnt(1)
	v_pk_add_f32 v[26:27], v[62:63], v[26:27]
	v_mov_b32_e32 v62, 0
	v_cvt_pk_fp8_f32 v62, v26, v27
	s_waitcnt vmcnt(13) lgkmcnt(0)
; #define PG8_WAIT_V(n) asm volatile("s_waitcnt vmcnt(" #n ")" ::: "memory")
; #define PG8_BAR __builtin_amdgcn_s_barrier()
; #define EPO_LOAD(dst, g) do { const size_t off_ = base + (size_t)(((g) >> 2) * 128 + ((g) & 3) * 16) * DM; \
;         _Pragma("unroll") for (int bj_ = 0; bj_ < 2; ++bj_) { dst[bj_][0] = *(const f32x4*)(X + off_ + bj_ * 128); dst[bj_][1] = *(const f32x4*)(X + off_ + bj_ * 128 + (size_t)8 * DM); } } while (0)
; template <class Epi, class Sched, bool GATHER, bool ALIGN_EPI, bool SP2, bool FP8>
; __device__ __forceinline__ void gemm_phase(LAS unsigned char* lds, const Gemm g, const Sched& S, const Epi& E) {
;     ...
;         if (!has_next) break;
; #pragma unroll
;         for (int a = 0; a < 2; ++a)
; #pragma unroll
;             for (int b = 0; b < 2; ++b)
; #pragma unroll
;                 for (int m = 0; m < 4; ++m)
; #pragma unroll
;                     for (int n = 0; n < 2; ++n) acc[a][b][m][n] = (f32x4){0.f, 0.f, 0.f, 0.f};
;         cur = nxt; cA = nA; cB = nB; ++ui;
;         vA0 = nvA0; vA1 = nvA1;
;         if constexpr (ALIGN_EPI) { if (wr == 1) PG8_BAR; }
;     }
;     PG8_WAIT_V(0);
;     if constexpr (!ALIGN_EPI) { if (wr == 0) PG8_BAR; }
;     PG8_BAR;
;     __device__ __forceinline__ void operator()(const f32x4 (&acc)[2][2][4][2], const pg8::Unit& u, const Pre&, int wr, int wc, int fr, int fq) const {
;     ...
;         EPO_LOAD(xa, 6); __builtin_amdgcn_sched_barrier(0); EPO_DO(xb, 5); __builtin_amdgcn_sched_barrier(0);
;         EPO_LOAD(xb, 7); __builtin_amdgcn_sched_barrier(0); EPO_DO(xa, 6); __builtin_amdgcn_sched_barrier(0);
;         EPO_DO(xb, 7);
	v_pk_add_f32 v[32:33], v[60:61], v[32:33]
	v_add_co_u32_e32 v60, vcc, s66, v148
	v_pk_add_f32 v[28:29], v[64:65], v[28:29]
	s_nop 0
	v_addc_co_u32_e32 v61, vcc, 0, v149, vcc
	global_store_dwordx4 v[60:61], v[26:29], off
	v_add_co_u32_e32 v60, vcc, s67, v148
	v_cvt_pk_fp8_f32 v62, v28, v29 op_sel:[0,0,1]
	s_nop 0
	v_addc_co_u32_e32 v61, vcc, 0, v149, vcc
	v_add_co_u32_e32 v28, vcc, s59, v146
	v_pk_add_f32 v[30:31], v[58:59], v[30:31]
	s_nop 0
	v_addc_co_u32_e32 v29, vcc, 0, v147, vcc
	global_store_dwordx4 v[60:61], v[30:33], off
	global_store_dword v[28:29], v62, off
	v_mov_b32_e32 v62, 0
	v_cvt_pk_fp8_f32 v62, v30, v31
	v_lshl_add_u64 v[26:27], v[146:147], 0, s[10:11]
	s_mov_b32 s10, 0x54000
	v_add_co_u32_e32 v28, vcc, s10, v146
	v_cvt_pk_fp8_f32 v62, v32, v33 op_sel:[0,0,1]
	s_nop 0
	v_addc_co_u32_e32 v29, vcc, 0, v147, vcc
	v_lshl_add_u64 v[58:59], v[148:149], 0, s[26:27]
	global_store_dword v[28:29], v62, off
	ds_write_b128 v154, v[22:25]
	ds_write_b128 v153, v[18:21]
	ds_read_b128 v[18:21], v152
	ds_read_b128 v[22:25], v152 offset:1024
	v_mov_b32_e32 v30, 0
	s_waitcnt lgkmcnt(1)
	v_pk_add_f32 v[20:21], v[56:57], v[20:21]
	v_pk_add_f32 v[18:19], v[54:55], v[18:19]
	s_waitcnt vmcnt(16) lgkmcnt(0)
	v_pk_add_f32 v[24:25], v[52:53], v[24:25]
	v_pk_add_f32 v[22:23], v[50:51], v[22:23]
	global_store_dwordx4 v[58:59], v[18:21], off offset:512
	global_store_dwordx4 v[60:61], v[22:25], off offset:512
	v_cvt_pk_fp8_f32 v30, v18, v19
	v_mov_b32_e32 v18, 0
	v_cvt_pk_fp8_f32 v18, v22, v23
	v_cvt_pk_fp8_f32 v30, v20, v21 op_sel:[0,0,1]
	v_cvt_pk_fp8_f32 v18, v24, v25 op_sel:[0,0,1]
	global_store_dword v[26:27], v30, off offset:128
	global_store_dword v[28:29], v18, off offset:128
	ds_write_b128 v154, v[14:17]
	ds_write_b128 v153, v[10:13]
	ds_read_b128 v[10:13], v152
	ds_read_b128 v[14:17], v152 offset:1024
	v_mov_b32_e32 v22, 0
	v_add_co_u32_e32 v20, vcc, s68, v148
	s_waitcnt vmcnt(11) lgkmcnt(1)
	v_pk_add_f32 v[10:11], v[46:47], v[10:11]
	v_pk_add_f32 v[12:13], v[48:49], v[12:13]
	v_cvt_pk_fp8_f32 v22, v10, v11
	v_addc_co_u32_e32 v21, vcc, 0, v149, vcc
	global_store_dwordx4 v[20:21], v[10:13], off
	v_add_co_u32_e32 v20, vcc, s69, v148
	v_cvt_pk_fp8_f32 v22, v12, v13 op_sel:[0,0,1]
	s_mov_b64 s[10:11], 0x58000
	v_addc_co_u32_e32 v21, vcc, 0, v149, vcc
	v_lshl_add_u64 v[10:11], v[146:147], 0, s[10:11]
	s_mov_b32 s10, 0x58000
	v_add_co_u32_e32 v12, vcc, s10, v146
	s_waitcnt vmcnt(10) lgkmcnt(0)
	v_pk_add_f32 v[16:17], v[44:45], v[16:17]
	v_pk_add_f32 v[14:15], v[42:43], v[14:15]
	v_addc_co_u32_e32 v13, vcc, 0, v147, vcc
	global_store_dwordx4 v[20:21], v[14:17], off
	global_store_dword v[12:13], v22, off
	v_mov_b32_e32 v22, 0
	v_cvt_pk_fp8_f32 v22, v14, v15
	s_mov_b32 s10, 0x5c000
	v_add_co_u32_e32 v12, vcc, s10, v146
	v_cvt_pk_fp8_f32 v22, v16, v17 op_sel:[0,0,1]
	s_nop 0
	v_addc_co_u32_e32 v13, vcc, 0, v147, vcc
	v_lshl_add_u64 v[18:19], v[148:149], 0, s[28:29]
	global_store_dword v[12:13], v22, off
	ds_write_b128 v154, v[6:9]
	ds_write_b128 v153, v[2:5]
	ds_read_b128 v[2:5], v152
	ds_read_b128 v[6:9], v152 offset:1024
	v_mov_b32_e32 v14, 0
	v_readlane_b32 s82, v244, 0
	s_and_b64 vcc, exec, s[0:1]
	s_waitcnt lgkmcnt(1)
	v_pk_add_f32 v[4:5], v[40:41], v[4:5]
	v_pk_add_f32 v[2:3], v[38:39], v[2:3]
	s_waitcnt vmcnt(12) lgkmcnt(0)
	v_pk_add_f32 v[8:9], v[36:37], v[8:9]
	v_pk_add_f32 v[6:7], v[34:35], v[6:7]
	global_store_dwordx4 v[18:19], v[2:5], off offset:512
	global_store_dwordx4 v[20:21], v[6:9], off offset:512
	v_cvt_pk_fp8_f32 v14, v2, v3
	v_mov_b32_e32 v2, 0
	v_cvt_pk_fp8_f32 v2, v6, v7
	s_mov_b32 s74, s31
	v_cvt_pk_fp8_f32 v14, v4, v5 op_sel:[0,0,1]
	s_mov_b32 s33, s30
	v_cvt_pk_fp8_f32 v2, v8, v9 op_sel:[0,0,1]
	s_mov_b32 s78, s71
	s_mov_b32 s77, s70
	v_readlane_b32 s83, v244, 1
	s_mov_b32 s94, s55
	global_store_dword v[10:11], v14, off offset:128
	global_store_dword v[12:13], v2, off offset:128
	s_cbranch_vccz .LBB0_701
	s_waitcnt vmcnt(0)
	s_cmpk_gt_u32 s34, 0xff
	s_cbranch_scc1 .LBB0_712
	s_barrier
